# speedup vs baseline: 1.0040x; 1.0040x over previous
_Z11attn_kernelPKDF16_S0_S0_PfPDF16_S1_:
	s_bfe_u32 s77, s2, 0x10008
	s_lshl_b32 s3, s2, 7
	s_lshr_b32 s4, s2, 2
	s_and_b32 s3, s3, 0x180
	s_and_b32 s4, s4, 0x3ffffffe
	s_add_i32 s3, s3, s4
	s_bfe_u32 s2, s2, 0x10002
	s_or_b32 s40, s3, s2
	s_mov_b32 s41, 0
	s_lshl_b64 s[2:3], s[40:41], 2
	s_getpc_b64 s[4:5]
	s_add_u32 s4, s4, g_tab@rel32@lo+4
	s_addc_u32 s5, s5, g_tab@rel32@hi+12
	s_add_u32 s42, s4, s2
	s_addc_u32 s43, s5, s3
	s_load_dword s12, s[42:43], 0x0
	s_load_dwordx4 s[4:7], s[0:1], 0x8
	s_load_dword s76, s[42:43], 0x1000
	s_load_dwordx2 s[80:81], s[0:1], 0x0
	s_load_dwordx4 s[84:87], s[0:1], 0x18
	s_load_dwordx2 s[88:89], s[0:1], 0x28
	v_lshlrev_b32_e32 v2, 4, v0
	s_movk_i32 s8, 0x70
	v_readfirstlane_b32 s3, v0
	s_waitcnt lgkmcnt(0)
	s_add_u32 s70, s4, 0x2000
	s_addc_u32 s71, s5, 0
	s_add_u32 s72, s6, 0x2000
	s_addc_u32 s73, s7, 0
	s_and_b32 s2, s12, 3
	s_lshl_b32 s10, s2, 19
	v_bitop3_b32 v10, v2, s8, v0 bitop3:0x48
	s_add_u32 s8, s6, s10
	s_addc_u32 s9, s7, 0
	s_lshr_b32 s13, s3, 6
	s_bfe_u32 s40, s12, 0x70007
	s_bfe_u32 s33, s12, 0x6000e
	v_and_b32_e32 v1, 0x1f80, v2
	s_add_u32 s10, s4, s10
	v_or_b32_e32 v50, v10, v1
	v_mov_b32_e32 v51, 0
	s_addc_u32 s11, s5, 0
	v_lshl_add_u64 v[52:53], s[10:11], 0, v[50:51]
	v_lshl_add_u64 v[54:55], s[8:9], 0, v[50:51]
	s_lshl_b32 s8, s40, 13
	s_mov_b32 s9, s41
	s_lshl_b32 s50, s13, 10
	v_lshl_add_u64 v[2:3], v[52:53], 0, s[8:9]
	s_mov_b32 m0, s50
	s_add_i32 s51, s50, 0x2000
	global_load_lds_dwordx4 v[2:3], off
	v_lshl_add_u64 v[2:3], v[54:55], 0, s[8:9]
	s_mov_b32 m0, s51
	s_cmp_eq_u32 s33, 0
	global_load_lds_dwordx4 v[2:3], off
	s_cbranch_scc1 .LBB2_30
	s_mov_b64 s[14:15], s[80:81]
	s_mov_b64 s[8:9], s[84:85]
	s_mov_b64 s[10:11], s[86:87]
	s_mov_b64 s[44:45], s[88:89]
	s_cmp_lt_u32 s13, 4
	s_cbranch_scc1 .Lattn_prio_lo
	s_cmp_eq_u32 s77, 0
	s_cbranch_scc1 .Lattn_prio_1
	s_setprio 3
	s_branch .Lattn_prio_done
.Lattn_prio_1:
	s_setprio 1
	s_branch .Lattn_prio_done
.Lattn_prio_lo:
	s_cmp_eq_u32 s77, 0
	s_cbranch_scc1 .Lattn_prio_done
	s_setprio 2
